# v31 + no wait on the scan's stage-free flag write before the state update
# speedup vs baseline: 1.0064x; 1.0012x over previous
.LBB0_557:
	v_add_u32_e32 v132, s6, v131
	ds_read_b128 v[138:141], v136 offset:16384
	ds_read_b128 v[114:117], v136 offset:17408
	ds_read_b128 v[82:85], v136 offset:18432
	ds_read_b128 v[70:73], v136 offset:19456
	ds_read_b128 v[142:145], v136 offset:20480
	ds_read_b128 v[118:121], v136 offset:21504
	ds_read_b128 v[86:89], v136 offset:22528
	ds_read_b128 v[74:77], v136 offset:23552
	ds_read_b128 v[146:149], v136 offset:24576
	ds_read_b128 v[122:125], v136 offset:25600
	ds_read_b128 v[90:93], v136 offset:26624
	ds_read_b128 v[78:81], v136 offset:27648
	ds_read_b128 v[150:153], v136 offset:28672
	ds_read_b128 v[126:129], v136 offset:29696
	ds_read_b128 v[94:97], v136 offset:30720
	ds_read_b128 v[66:69], v136 offset:31744
	ds_read_b128 v[154:157], v132 offset:45056
	ds_read_b128 v[158:161], v132 offset:45088
	ds_read_b128 v[162:165], v132 offset:45120
	ds_read_b128 v[166:169], v132 offset:45152
	ds_read_b128 v[170:173], v132 offset:45184
	ds_read_b128 v[174:177], v132 offset:45216
	ds_read_b128 v[178:181], v132 offset:45248
	ds_read_b128 v[182:185], v132 offset:45280
	ds_read_b128 v[186:189], v132 offset:45312
	ds_read_b128 v[190:193], v132 offset:45344
	ds_read_b128 v[198:201], v132 offset:45376
	ds_read_b128 v[202:205], v132 offset:45408
	ds_read_b128 v[206:209], v132 offset:45440
	ds_read_b128 v[210:213], v132 offset:45472
	ds_read_b128 v[214:217], v132 offset:45504
	ds_read_b128 v[218:221], v132 offset:45536
	s_add_i32 s10, s10, 1
	s_waitcnt lgkmcnt(0)
	v_mov_b32_e32 v132, s17
	v_mov_b32_e32 v136, s10
	ds_write_b32 v132, v136
	v_pk_mul_f32 v[2:3], v[2:3], v[154:155]
	v_pk_mul_f32 v[4:5], v[4:5], v[156:157]
	v_pk_mul_f32 v[6:7], v[6:7], v[158:159]
	v_pk_mul_f32 v[8:9], v[8:9], v[160:161]
	v_pk_mul_f32 v[10:11], v[10:11], v[162:163]
	v_pk_mul_f32 v[12:13], v[12:13], v[164:165]
	v_pk_mul_f32 v[14:15], v[14:15], v[166:167]
	v_pk_mul_f32 v[16:17], v[16:17], v[168:169]
	v_pk_mul_f32 v[18:19], v[18:19], v[170:171]
	v_pk_mul_f32 v[20:21], v[20:21], v[172:173]
	v_pk_mul_f32 v[22:23], v[22:23], v[174:175]
	v_pk_mul_f32 v[24:25], v[24:25], v[176:177]
	v_pk_mul_f32 v[26:27], v[26:27], v[178:179]
	v_pk_mul_f32 v[28:29], v[28:29], v[180:181]
	v_pk_mul_f32 v[30:31], v[30:31], v[182:183]
	v_pk_mul_f32 v[32:33], v[32:33], v[184:185]
	v_pk_mul_f32 v[34:35], v[34:35], v[186:187]
	v_pk_mul_f32 v[36:37], v[36:37], v[188:189]
	v_pk_mul_f32 v[38:39], v[38:39], v[190:191]
	v_pk_mul_f32 v[40:41], v[40:41], v[192:193]
	v_pk_mul_f32 v[42:43], v[42:43], v[198:199]
	v_pk_mul_f32 v[44:45], v[44:45], v[200:201]
	v_pk_mul_f32 v[46:47], v[46:47], v[202:203]
	v_pk_mul_f32 v[48:49], v[48:49], v[204:205]
	v_pk_mul_f32 v[50:51], v[50:51], v[206:207]
	v_pk_mul_f32 v[52:53], v[52:53], v[208:209]
	v_pk_mul_f32 v[54:55], v[54:55], v[210:211]
	v_pk_mul_f32 v[56:57], v[56:57], v[212:213]
	v_pk_mul_f32 v[58:59], v[58:59], v[214:215]
	v_pk_mul_f32 v[60:61], v[60:61], v[216:217]
	v_pk_mul_f32 v[62:63], v[62:63], v[218:219]
	v_pk_mul_f32 v[64:65], v[64:65], v[220:221]
	v_mfma_f32_32x32x16_bf16 v[2:17], v[138:141], v[110:113], v[2:17]
	s_cmpk_eq_i32 s10, 0x44
	v_mfma_f32_32x32x16_bf16 v[18:33], v[142:145], v[110:113], v[18:33]
	v_mfma_f32_32x32x16_bf16 v[34:49], v[146:149], v[110:113], v[34:49]
	v_mfma_f32_32x32x16_bf16 v[50:65], v[150:153], v[110:113], v[50:65]
	v_mfma_f32_32x32x16_bf16 v[2:17], v[114:117], v[106:109], v[2:17]
	v_mfma_f32_32x32x16_bf16 v[18:33], v[118:121], v[106:109], v[18:33]
	v_mfma_f32_32x32x16_bf16 v[34:49], v[122:125], v[106:109], v[34:49]
	v_mfma_f32_32x32x16_bf16 v[50:65], v[126:129], v[106:109], v[50:65]
	v_mfma_f32_32x32x16_bf16 v[2:17], v[82:85], v[102:105], v[2:17]
	v_mfma_f32_32x32x16_bf16 v[18:33], v[86:89], v[102:105], v[18:33]
	v_mfma_f32_32x32x16_bf16 v[34:49], v[90:93], v[102:105], v[34:49]
	v_mfma_f32_32x32x16_bf16 v[50:65], v[94:97], v[102:105], v[50:65]
	v_mfma_f32_32x32x16_bf16 v[2:17], v[70:73], v[98:101], v[2:17]
	v_mfma_f32_32x32x16_bf16 v[18:33], v[74:77], v[98:101], v[18:33]
	v_mfma_f32_32x32x16_bf16 v[34:49], v[78:81], v[98:101], v[34:49]
	v_mfma_f32_32x32x16_bf16 v[50:65], v[66:69], v[98:101], v[50:65]
	s_cbranch_scc1 .LBB0_573
